# norm2 phase: next row of the residual stream touched (prefetched into cache) while the current row is normalised
# speedup vs baseline: 1.0020x; 1.0020x over previous
.LBB0_1171:
	s_ashr_i32 s1, s0, 31
	s_lshl_b64 s[14:15], s[0:1], 12
	s_ashr_i32 s1, s0, 13
	s_mul_hi_i32 s9, s1, 0x34000
	s_mul_i32 s1, s1, 0x34000
	s_add_u32 s34, s2, s1
	v_lshl_add_u64 v[0:1], v[8:9], 0, s[14:15]
	s_addc_u32 s35, s4, s9
	global_load_dwordx2 v[26:27], v[0:1], off
	global_load_dwordx2 v[28:29], v[0:1], off offset:512
	global_load_dwordx2 v[30:31], v[0:1], off offset:1024
	global_load_dwordx2 v[32:33], v[0:1], off offset:1536
	global_load_dwordx2 v[34:35], v[0:1], off offset:2048
	global_load_dwordx2 v[74:75], v[0:1], off offset:2560
	global_load_dwordx2 v[76:77], v[0:1], off offset:3072
	global_load_dwordx2 v[78:79], v[0:1], off offset:3584
	v_mov_b32_e32 v228, s8
	v_lshlrev_b32_e32 v228, 12, v228
	v_mov_b32_e32 v229, 0
	v_lshl_add_u64 v[228:229], v[0:1], 0, v[228:229]
	s_add_u32 s28, s5, s1
	s_addc_u32 s29, s6, s9
	global_load_dwordx4 v[0:3], v[10:11], off
	global_load_dwordx4 v[4:7], v68, s[34:35]
	global_load_dwordx4 v[22:25], v68, s[28:29]
	global_load_dwordx4 v[100:103], v[10:11], off offset:1024
	global_load_dwordx4 v[104:107], v68, s[34:35] offset:1024
	global_load_dwordx4 v[174:177], v68, s[28:29] offset:1024
	global_load_dwordx4 v[108:111], v[10:11], off offset:2048
	global_load_dwordx4 v[112:115], v68, s[34:35] offset:2048
	global_load_dwordx4 v[178:181], v68, s[28:29] offset:2048
	global_load_dwordx4 v[116:119], v[10:11], off offset:3072
	global_load_dwordx4 v[120:123], v68, s[34:35] offset:3072
	global_load_dwordx4 v[182:185], v68, s[28:29] offset:3072
	global_load_dwordx4 v[124:127], v[12:13], off
	global_load_dwordx4 v[128:131], v69, s[34:35]
	global_load_dwordx4 v[186:189], v69, s[28:29]
	global_load_dwordx4 v[132:135], v[14:15], off
	global_load_dwordx4 v[136:139], v70, s[34:35]
	global_load_dwordx4 v[190:193], v70, s[28:29]
	global_load_dwordx4 v[140:143], v[16:17], off
	global_load_dwordx4 v[144:147], v71, s[34:35]
	global_load_dwordx4 v[194:197], v71, s[28:29]
	global_load_dwordx4 v[148:151], v[18:19], off
	global_load_dwordx4 v[152:155], v72, s[34:35]
	global_load_dwordx4 v[198:201], v72, s[28:29]
	global_load_dword v230, v[228:229], off
	global_load_dword v230, v[228:229], off offset:512
	global_load_dword v230, v[228:229], off offset:1024
	global_load_dword v230, v[228:229], off offset:1536
	global_load_dword v230, v[228:229], off offset:2048
	global_load_dword v230, v[228:229], off offset:2560
	global_load_dword v230, v[228:229], off offset:3072
	global_load_dword v230, v[228:229], off offset:3584
	s_add_i32 s0, s0, s8
	s_cmpk_lt_i32 s0, 0x4000
	s_waitcnt vmcnt(39)
	v_lshlrev_b32_e32 v54, 16, v26
	v_and_b32_e32 v55, 0xffff0000, v26
	v_lshlrev_b32_e32 v48, 16, v27
	v_and_b32_e32 v49, 0xffff0000, v27
	v_pk_mul_f32 v[62:63], v[54:55], v[54:55]
	s_waitcnt vmcnt(38)
	v_lshlrev_b32_e32 v60, 16, v28
	v_and_b32_e32 v61, 0xffff0000, v28
	v_pk_mul_f32 v[58:59], v[48:49], v[48:49]
	v_lshlrev_b32_e32 v50, 16, v29
	v_and_b32_e32 v51, 0xffff0000, v29
	v_pk_mul_f32 v[82:83], v[60:61], v[60:61]
	s_waitcnt vmcnt(37)
	v_lshlrev_b32_e32 v46, 16, v30
	v_and_b32_e32 v47, 0xffff0000, v30
	s_waitcnt vmcnt(36)
	v_lshlrev_b32_e32 v40, 16, v33
	v_and_b32_e32 v41, 0xffff0000, v33
	s_waitcnt vmcnt(35)
	v_and_b32_e32 v39, 0xffff0000, v34
	s_waitcnt vmcnt(34)
	v_and_b32_e32 v33, 0xffff0000, v74
	v_add_f32_e32 v62, v62, v63
	v_pk_mul_f32 v[80:81], v[50:51], v[50:51]
	v_lshlrev_b32_e32 v44, 16, v31
	v_and_b32_e32 v45, 0xffff0000, v31
	v_pk_mul_f32 v[66:67], v[46:47], v[46:47]
	v_lshlrev_b32_e32 v42, 16, v32
	v_and_b32_e32 v43, 0xffff0000, v32
	v_lshlrev_b32_e32 v36, 16, v35
	v_and_b32_e32 v37, 0xffff0000, v35
	v_lshlrev_b32_e32 v38, 16, v34
	v_lshlrev_b32_e32 v32, 16, v74
	v_mov_b32_e32 v34, v39
	v_mov_b32_e32 v35, v33
	v_add_f32_e32 v73, v82, v83
	v_add_f32_e32 v58, v58, v62
	v_pk_mul_f32 v[64:65], v[44:45], v[44:45]
	v_lshlrev_b32_e32 v28, 16, v75
	v_mov_b32_e32 v30, v38
	v_mov_b32_e32 v31, v32
	v_pk_mul_f32 v[34:35], v[34:35], v[34:35]
	v_add_f32_e32 v73, v80, v73
	v_add_f32_e32 v58, v59, v58
	v_add_f32_e32 v59, v66, v67
	s_waitcnt vmcnt(29)
	v_pk_add_f32 v[52:53], v[24:25], 1.0 op_sel_hi:[1,0]
	v_and_b32_e32 v29, 0xffff0000, v75
	v_mov_b32_e32 v24, v36
	v_mov_b32_e32 v25, v28
	v_pk_fma_f32 v[30:31], v[30:31], v[30:31], v[34:35]
	v_add_f32_e32 v73, v81, v73
	v_add_f32_e32 v59, v64, v59
	v_pk_mul_f32 v[86:87], v[42:43], v[42:43]
	v_mov_b32_e32 v26, v37
	v_mov_b32_e32 v27, v29
	v_pk_fma_f32 v[24:25], v[24:25], v[24:25], v[30:31]
	v_add_f32_e32 v58, v58, v73
	v_add_f32_e32 v59, v65, v59
	v_pk_mul_f32 v[84:85], v[40:41], v[40:41]
	v_pk_fma_f32 v[74:75], v[26:27], v[26:27], v[24:25]
	v_and_b32_e32 v35, 0xffff0000, v76
	v_and_b32_e32 v27, 0xffff0000, v78
	v_add_f32_e32 v58, v58, v59
	v_add_f32_e32 v59, v86, v87
	v_lshlrev_b32_e32 v34, 16, v76
	v_lshlrev_b32_e32 v26, 16, v78
	v_mov_b32_e32 v90, v35
	v_mov_b32_e32 v91, v27
	v_add_f32_e32 v59, v84, v59
	v_lshlrev_b32_e32 v30, 16, v77
	v_lshlrev_b32_e32 v24, 16, v79
	v_mov_b32_e32 v88, v34
	v_mov_b32_e32 v89, v26
	v_pk_mul_f32 v[90:91], v[90:91], v[90:91]
	v_add_f32_e32 v59, v85, v59
	v_and_b32_e32 v31, 0xffff0000, v77
	v_and_b32_e32 v25, 0xffff0000, v79
	v_mov_b32_e32 v76, v30
	v_mov_b32_e32 v77, v24
	v_pk_fma_f32 v[88:89], v[88:89], v[88:89], v[90:91]
	v_add_f32_e32 v58, v58, v59
	v_mov_b32_e32 v78, v31
	v_mov_b32_e32 v79, v25
	v_pk_fma_f32 v[76:77], v[76:77], v[76:77], v[88:89]
	v_add_f32_e32 v58, v58, v74
	v_pk_fma_f32 v[76:77], v[78:79], v[78:79], v[76:77]
	v_add_f32_e32 v58, v58, v75
	v_add_f32_e32 v58, v58, v76
	v_add_f32_e32 v58, v58, v77
	v_mov_b32_e32 v59, v97
	v_pk_add_f32 v[56:57], v[22:23], 1.0 op_sel_hi:[1,0]
	v_add_f32_dpp v58, v58, v58 quad_perm:[1,0,3,2] row_mask:0xf bank_mask:0xf bound_ctrl:1
	v_lshl_add_u64 v[22:23], v[20:21], 0, s[14:15]
	s_nop 0
	v_add_f32_dpp v58, v58, v58 quad_perm:[2,3,0,1] row_mask:0xf bank_mask:0xf bound_ctrl:1
	s_nop 1
	v_add_f32_dpp v58, v58, v58 row_half_mirror row_mask:0xf bank_mask:0xf bound_ctrl:1
	s_nop 1
	v_add_f32_dpp v58, v58, v58 row_mirror row_mask:0xf bank_mask:0xf bound_ctrl:1
	s_nop 1
	v_mov_b32_dpp v59, v58 row_bcast:15 row_mask:0xa bank_mask:0xf
	v_add_f32_e32 v58, v58, v59
	v_mov_b32_e32 v59, v97
	s_nop 1
	v_mov_b32_dpp v59, v58 row_bcast:31 row_mask:0xc bank_mask:0xf
	v_add_f32_e32 v58, v58, v59
	s_nop 0
	v_readlane_b32 s1, v58, 63
	s_nop 1
	v_fma_f32 v58, s1, v217, v205
	v_cmp_gt_f32_e32 vcc, s17, v58
	v_mul_f32_e32 v59, 0x4b800000, v58
	s_nop 0
	v_cndmask_b32_e32 v58, v58, v59, vcc
	v_rsq_f32_e32 v58, v58
	s_nop 0
	v_mul_f32_e32 v59, 0x45800000, v58
	v_cndmask_b32_e32 v58, v58, v59, vcc
	v_pk_mul_f32 v[54:55], v[58:59], v[54:55] op_sel_hi:[0,1]
	v_pk_mul_f32 v[0:1], v[0:1], v[54:55]
	v_pk_mul_f32 v[46:47], v[58:59], v[46:47] op_sel_hi:[0,1]
	v_pk_fma_f32 v[0:1], v[56:57], v[0:1], v[4:5]
	v_pk_mul_f32 v[4:5], v[58:59], v[48:49] op_sel_hi:[0,1]
	v_pk_mul_f32 v[2:3], v[2:3], v[4:5]
	v_cvt_pk_bf16_f32 v0, v0, v1
	v_pk_fma_f32 v[2:3], v[52:53], v[2:3], v[6:7]
	v_pk_mul_f32 v[48:49], v[58:59], v[60:61] op_sel_hi:[0,1]
	v_cvt_pk_bf16_f32 v1, v2, v3
	global_store_dwordx2 v[22:23], v[0:1], off
	v_pk_mul_f32 v[42:43], v[58:59], v[42:43] op_sel_hi:[0,1]
	v_pk_mul_f32 v[38:39], v[58:59], v[38:39] op_sel_hi:[0,1]
	v_pk_mul_f32 v[32:33], v[58:59], v[32:33] op_sel_hi:[0,1]
	v_pk_mul_f32 v[26:27], v[58:59], v[26:27] op_sel_hi:[0,1]
	s_waitcnt vmcnt(27)
	v_pk_mul_f32 v[0:1], v[100:101], v[48:49]
	v_pk_add_f32 v[48:49], v[174:175], 1.0 op_sel_hi:[1,0]
	s_nop 0
	v_pk_fma_f32 v[0:1], v[48:49], v[0:1], v[104:105]
	v_pk_mul_f32 v[4:5], v[58:59], v[50:51] op_sel_hi:[0,1]
	v_pk_mul_f32 v[2:3], v[102:103], v[4:5]
	v_pk_add_f32 v[4:5], v[176:177], 1.0 op_sel_hi:[1,0]
	v_cvt_pk_bf16_f32 v0, v0, v1
	v_pk_fma_f32 v[2:3], v[4:5], v[2:3], v[106:107]
	s_nop 0
	v_cvt_pk_bf16_f32 v1, v2, v3
	global_store_dwordx2 v[22:23], v[0:1], off offset:512
	s_waitcnt vmcnt(25)
	v_pk_mul_f32 v[0:1], v[46:47], v[108:109]
	v_pk_add_f32 v[46:47], v[178:179], 1.0 op_sel_hi:[1,0]
	s_nop 0
	v_pk_fma_f32 v[0:1], v[0:1], v[46:47], v[112:113]
	v_pk_mul_f32 v[4:5], v[58:59], v[44:45] op_sel_hi:[0,1]
	v_pk_mul_f32 v[2:3], v[4:5], v[110:111]
	v_pk_add_f32 v[4:5], v[180:181], 1.0 op_sel_hi:[1,0]
	v_cvt_pk_bf16_f32 v0, v0, v1
	v_pk_fma_f32 v[2:3], v[2:3], v[4:5], v[114:115]
	s_nop 0
	v_cvt_pk_bf16_f32 v1, v2, v3
	global_store_dwordx2 v[22:23], v[0:1], off offset:1024
	s_waitcnt vmcnt(23)
	v_pk_mul_f32 v[0:1], v[42:43], v[116:117]
	v_pk_add_f32 v[42:43], v[182:183], 1.0 op_sel_hi:[1,0]
	s_nop 0
	v_pk_fma_f32 v[0:1], v[0:1], v[42:43], v[120:121]
	v_pk_mul_f32 v[4:5], v[58:59], v[40:41] op_sel_hi:[0,1]
	v_pk_mul_f32 v[2:3], v[4:5], v[118:119]
	v_pk_add_f32 v[4:5], v[184:185], 1.0 op_sel_hi:[1,0]
	v_cvt_pk_bf16_f32 v0, v0, v1
	v_pk_fma_f32 v[2:3], v[2:3], v[4:5], v[122:123]
	s_nop 0
	v_cvt_pk_bf16_f32 v1, v2, v3
	global_store_dwordx2 v[22:23], v[0:1], off offset:1536
	s_waitcnt vmcnt(21)
	v_pk_mul_f32 v[0:1], v[38:39], v[124:125]
	v_pk_add_f32 v[38:39], v[186:187], 1.0 op_sel_hi:[1,0]
	s_nop 0
	v_pk_fma_f32 v[0:1], v[0:1], v[38:39], v[128:129]
	v_pk_mul_f32 v[4:5], v[58:59], v[36:37] op_sel_hi:[0,1]
	v_pk_mul_f32 v[2:3], v[4:5], v[126:127]
	v_pk_add_f32 v[4:5], v[188:189], 1.0 op_sel_hi:[1,0]
	v_cvt_pk_bf16_f32 v0, v0, v1
	v_pk_fma_f32 v[2:3], v[2:3], v[4:5], v[130:131]
	s_nop 0
	v_cvt_pk_bf16_f32 v1, v2, v3
	global_store_dwordx2 v[22:23], v[0:1], off offset:2048
	s_waitcnt vmcnt(19)
	v_pk_mul_f32 v[0:1], v[32:33], v[132:133]
	v_pk_add_f32 v[32:33], v[190:191], 1.0 op_sel_hi:[1,0]
	s_nop 0
	v_pk_fma_f32 v[0:1], v[0:1], v[32:33], v[136:137]
	v_pk_mul_f32 v[4:5], v[58:59], v[28:29] op_sel_hi:[0,1]
	v_pk_mul_f32 v[2:3], v[4:5], v[134:135]
	v_pk_add_f32 v[4:5], v[192:193], 1.0 op_sel_hi:[1,0]
	v_cvt_pk_bf16_f32 v0, v0, v1
	v_pk_fma_f32 v[2:3], v[2:3], v[4:5], v[138:139]
	v_pk_mul_f32 v[28:29], v[58:59], v[34:35] op_sel_hi:[0,1]
	v_cvt_pk_bf16_f32 v1, v2, v3
	global_store_dwordx2 v[22:23], v[0:1], off offset:2560
	s_waitcnt vmcnt(17)
	v_pk_mul_f32 v[0:1], v[28:29], v[140:141]
	v_pk_add_f32 v[28:29], v[194:195], 1.0 op_sel_hi:[1,0]
	s_nop 0
	v_pk_fma_f32 v[0:1], v[0:1], v[28:29], v[144:145]
	v_pk_mul_f32 v[4:5], v[58:59], v[30:31] op_sel_hi:[0,1]
	v_pk_mul_f32 v[2:3], v[4:5], v[142:143]
	v_pk_add_f32 v[4:5], v[196:197], 1.0 op_sel_hi:[1,0]
	v_cvt_pk_bf16_f32 v0, v0, v1
	v_pk_fma_f32 v[2:3], v[2:3], v[4:5], v[146:147]
	s_nop 0
	v_cvt_pk_bf16_f32 v1, v2, v3
	global_store_dwordx2 v[22:23], v[0:1], off offset:3072
	s_waitcnt vmcnt(15)
	v_pk_mul_f32 v[0:1], v[26:27], v[148:149]
	v_pk_add_f32 v[26:27], v[198:199], 1.0 op_sel_hi:[1,0]
	s_nop 0
	v_pk_fma_f32 v[0:1], v[0:1], v[26:27], v[152:153]
	v_pk_mul_f32 v[4:5], v[58:59], v[24:25] op_sel_hi:[0,1]
	v_pk_mul_f32 v[2:3], v[4:5], v[150:151]
	v_pk_add_f32 v[4:5], v[200:201], 1.0 op_sel_hi:[1,0]
	v_cvt_pk_bf16_f32 v0, v0, v1
	v_pk_fma_f32 v[2:3], v[2:3], v[4:5], v[154:155]
	s_nop 0
	v_cvt_pk_bf16_f32 v1, v2, v3
	global_store_dwordx2 v[22:23], v[0:1], off offset:3584
	s_cbranch_scc1 .LBB0_1171
